# v27 + P6 K-loop LDS-DMA in saddr + 32-bit offset form (14 v_lshl_add_u64 removed)
# speedup vs baseline: 1.0098x; 1.0036x over previous
.LBB0_594:
	ds_read_b128 v[24:27], v186
	ds_read_b128 v[28:31], v186 offset:1024
	ds_read_b128 v[16:19], v186 offset:2048
	ds_read_b128 v[20:23], v186 offset:3072
	ds_read_b128 v[8:11], v187
	ds_read_b128 v[12:15], v187 offset:1024
	ds_read_b128 v[0:3], v187 offset:2048
	ds_read_b128 v[4:7], v187 offset:3072
	s_add_i32 m0, s31, 0xc000
	ds_read_b128 v[192:195], v188
	ds_read_b128 v[196:199], v188 offset:1024
	ds_read_b128 v[200:203], v188 offset:2048
	ds_read_b128 v[204:207], v188 offset:3072
	ds_read_b128 v[208:211], v188 offset:4096
	ds_read_b128 v[212:215], v188 offset:5120
	ds_read_b128 v[224:227], v188 offset:6144
	ds_read_b128 v[228:231], v188 offset:7168
	global_load_lds_dwordx4 v[178:179], off
	s_add_i32 m0, s31, 0xe000
	s_nop 0
	global_load_lds_dwordx4 v[180:181], off
	s_waitcnt vmcnt(8)
	s_waitcnt lgkmcnt(0)
	s_barrier
	s_setprio 1
	s_waitcnt lgkmcnt(0)
	v_mfma_f32_16x16x128_f8f6f4 v[156:159], v[24:31], v[192:199], v[156:159]
	v_mfma_f32_16x16x128_f8f6f4 v[148:151], v[16:23], v[192:199], v[148:151]
	v_mfma_f32_16x16x128_f8f6f4 v[140:143], v[24:31], v[200:207], v[140:143]
	v_mfma_f32_16x16x128_f8f6f4 v[132:135], v[16:23], v[200:207], v[132:135]
	v_mfma_f32_16x16x128_f8f6f4 v[124:127], v[24:31], v[208:215], v[124:127]
	v_mfma_f32_16x16x128_f8f6f4 v[116:119], v[16:23], v[208:215], v[116:119]
	v_mfma_f32_16x16x128_f8f6f4 v[108:111], v[24:31], v[224:231], v[108:111]
	v_mfma_f32_16x16x128_f8f6f4 v[100:103], v[16:23], v[224:231], v[100:103]
	s_setprio 0
	s_setprio 1
	v_mfma_f32_16x16x128_f8f6f4 v[152:155], v[8:15], v[192:199], v[152:155]
	v_mfma_f32_16x16x128_f8f6f4 v[144:147], v[0:7], v[192:199], v[144:147]
	v_mfma_f32_16x16x128_f8f6f4 v[136:139], v[8:15], v[200:207], v[136:139]
	v_mfma_f32_16x16x128_f8f6f4 v[128:131], v[0:7], v[200:207], v[128:131]
	v_mfma_f32_16x16x128_f8f6f4 v[120:123], v[8:15], v[208:215], v[120:123]
	v_mfma_f32_16x16x128_f8f6f4 v[112:115], v[0:7], v[208:215], v[112:115]
	v_mfma_f32_16x16x128_f8f6f4 v[104:107], v[8:15], v[224:231], v[104:107]
	v_mfma_f32_16x16x128_f8f6f4 v[96:99], v[0:7], v[224:231], v[96:99]
	s_setprio 0
	s_barrier
	s_cmp_gt_u32 s15, 5
	s_cselect_b64 s[36:37], -1, 0
	s_and_b64 s[40:41], s[36:37], exec
	v_sub_co_u32_e64 v216, s[40:41], s15, 6
	s_nop 0
	v_readfirstlane_b32 s73, v216
	s_cselect_b32 s17, s27, s39
	s_cselect_b32 s67, s26, s38
	s_add_i32 s76, s73, 8
	s_and_b64 s[74:75], s[36:37], exec
	s_cselect_b32 s74, s73, s76
	s_ashr_i32 s75, s74, 31
	s_lshl_b64 s[74:75], s[74:75], 7
	s_add_u32 s76, s67, s74
	s_addc_u32 s77, s17, s75
	s_add_i32 s17, s61, s29
	s_mov_b32 m0, s17
	ds_read_b128 v[192:195], v188 offset:16384
	ds_read_b128 v[196:199], v188 offset:17408
	ds_read_b128 v[200:203], v188 offset:18432
	ds_read_b128 v[204:207], v188 offset:19456
	ds_read_b128 v[208:211], v188 offset:20480
	ds_read_b128 v[212:215], v188 offset:21504
	ds_read_b128 v[224:227], v188 offset:22528
	ds_read_b128 v[228:231], v188 offset:23552
	global_load_lds_dwordx4 v162, s[76:77]
	s_add_i32 m0, s17, 0x2000
	s_add_i32 s17, s62, s29
	global_load_lds_dwordx4 v166, s[76:77]
	s_add_u32 s76, s76, 0x20000
	s_addc_u32 s77, s77, 0
	s_mov_b32 m0, s17
	s_nop 0
	global_load_lds_dwordx4 v162, s[76:77]
	s_add_i32 m0, s17, 0x2000
	s_and_b64 s[36:37], s[36:37], exec
	s_cselect_b32 s36, s22, s34
	s_cselect_b32 s17, s23, s35
	s_add_u32 s36, s36, s74
	s_addc_u32 s37, s17, s75
	global_load_lds_dwordx4 v166, s[76:77]
	s_mov_b32 m0, s31
	s_nop 0
	global_load_lds_dwordx4 v160, s[36:37]
	s_mov_b32 m0, s49
	s_nop 0
	global_load_lds_dwordx4 v164, s[36:37]
	s_waitcnt vmcnt(8)
	s_waitcnt lgkmcnt(0)
	s_barrier
	s_setprio 1
	s_waitcnt lgkmcnt(0)
	v_mfma_f32_16x16x128_f8f6f4 v[92:95], v[24:31], v[192:199], v[92:95]
	v_mfma_f32_16x16x128_f8f6f4 v[84:87], v[16:23], v[192:199], v[84:87]
	v_mfma_f32_16x16x128_f8f6f4 v[76:79], v[24:31], v[200:207], v[76:79]
	v_mfma_f32_16x16x128_f8f6f4 v[64:67], v[16:23], v[200:207], v[64:67]
	v_mfma_f32_16x16x128_f8f6f4 v[52:55], v[24:31], v[208:215], v[52:55]
	v_mfma_f32_16x16x128_f8f6f4 v[44:47], v[16:23], v[208:215], v[44:47]
	v_mfma_f32_16x16x128_f8f6f4 v[36:39], v[24:31], v[224:231], v[36:39]
	v_mfma_f32_16x16x128_f8f6f4 v[32:35], v[16:23], v[224:231], v[32:35]
	s_setprio 0
	s_setprio 1
	v_mfma_f32_16x16x128_f8f6f4 v[88:91], v[8:15], v[192:199], v[88:91]
	v_mfma_f32_16x16x128_f8f6f4 v[80:83], v[0:7], v[192:199], v[80:83]
	v_mfma_f32_16x16x128_f8f6f4 v[68:71], v[8:15], v[200:207], v[68:71]
	v_mfma_f32_16x16x128_f8f6f4 v[56:59], v[0:7], v[200:207], v[56:59]
	v_mfma_f32_16x16x128_f8f6f4 v[72:75], v[8:15], v[208:215], v[72:75]
	v_mfma_f32_16x16x128_f8f6f4 v[60:63], v[0:7], v[208:215], v[60:63]
	v_mfma_f32_16x16x128_f8f6f4 v[48:51], v[8:15], v[224:231], v[48:51]
	v_mfma_f32_16x16x128_f8f6f4 v[40:43], v[0:7], v[224:231], v[40:43]
	s_setprio 0
	s_barrier
	s_add_i32 s17, 0, 0x18000
	s_add_i32 s67, 0, 0x1c000
	v_add_u32_e32 v0, s17, v183
	v_add_u32_e32 v4, s67, v183
	ds_read_b128 v[24:27], v0
	ds_read_b128 v[28:31], v0 offset:1024
	ds_read_b128 v[16:19], v0 offset:2048
	ds_read_b128 v[20:23], v0 offset:3072
	ds_read_b128 v[8:11], v4
	ds_read_b128 v[12:15], v4 offset:1024
	ds_read_b128 v[0:3], v4 offset:2048
	ds_read_b128 v[4:7], v4 offset:3072
	s_add_u32 s36, s36, 0x20000
	s_addc_u32 s37, s37, 0
	s_mov_b32 m0, s50
	ds_read_b128 v[192:195], v188 offset:32768
	ds_read_b128 v[196:199], v188 offset:33792
	ds_read_b128 v[200:203], v188 offset:34816
	ds_read_b128 v[204:207], v188 offset:35840
	ds_read_b128 v[208:211], v188 offset:36864
	ds_read_b128 v[212:215], v188 offset:37888
	ds_read_b128 v[224:227], v188 offset:38912
	ds_read_b128 v[228:231], v188 offset:39936
	global_load_lds_dwordx4 v160, s[36:37]
	s_mov_b32 m0, s51
	s_nop 0
	global_load_lds_dwordx4 v164, s[36:37]
	s_waitcnt vmcnt(8)
	s_waitcnt lgkmcnt(0)
	s_barrier
	s_setprio 1
	s_waitcnt lgkmcnt(0)
	v_mfma_f32_16x16x128_f8f6f4 v[156:159], v[24:31], v[192:199], v[156:159]
	v_mfma_f32_16x16x128_f8f6f4 v[148:151], v[16:23], v[192:199], v[148:151]
	v_mfma_f32_16x16x128_f8f6f4 v[140:143], v[24:31], v[200:207], v[140:143]
	v_mfma_f32_16x16x128_f8f6f4 v[132:135], v[16:23], v[200:207], v[132:135]
	v_mfma_f32_16x16x128_f8f6f4 v[124:127], v[24:31], v[208:215], v[124:127]
	v_mfma_f32_16x16x128_f8f6f4 v[116:119], v[16:23], v[208:215], v[116:119]
	v_mfma_f32_16x16x128_f8f6f4 v[108:111], v[24:31], v[224:231], v[108:111]
	v_mfma_f32_16x16x128_f8f6f4 v[100:103], v[16:23], v[224:231], v[100:103]
	s_setprio 0
	s_setprio 1
	v_mfma_f32_16x16x128_f8f6f4 v[152:155], v[8:15], v[192:199], v[152:155]
	v_mfma_f32_16x16x128_f8f6f4 v[144:147], v[0:7], v[192:199], v[144:147]
	v_mfma_f32_16x16x128_f8f6f4 v[136:139], v[8:15], v[200:207], v[136:139]
	v_mfma_f32_16x16x128_f8f6f4 v[128:131], v[0:7], v[200:207], v[128:131]
	v_mfma_f32_16x16x128_f8f6f4 v[120:123], v[8:15], v[208:215], v[120:123]
	v_mfma_f32_16x16x128_f8f6f4 v[112:115], v[0:7], v[208:215], v[112:115]
	v_mfma_f32_16x16x128_f8f6f4 v[104:107], v[8:15], v[224:231], v[104:107]
	v_mfma_f32_16x16x128_f8f6f4 v[96:99], v[0:7], v[224:231], v[96:99]
	s_setprio 0
	s_barrier
	s_cmp_gt_u32 s15, 4
	s_cselect_b64 s[36:37], -1, 0
	s_and_b64 s[74:75], s[36:37], exec
	s_cselect_b32 s74, -5, 3
	s_cselect_b32 s73, s27, s39
	s_cselect_b32 s76, s26, s38
	s_add_i32 s74, s74, s15
	s_ashr_i32 s75, s74, 31
	s_lshl_b64 s[74:75], s[74:75], 7
	s_add_u32 s76, s76, s74
	s_addc_u32 s77, s73, s75
	s_add_i32 s17, s17, s29
	s_mov_b32 m0, s17
	ds_read_b128 v[192:195], v188 offset:49152
	ds_read_b128 v[196:199], v188 offset:50176
	ds_read_b128 v[200:203], v188 offset:51200
	ds_read_b128 v[204:207], v188 offset:52224
	ds_read_b128 v[208:211], v188 offset:53248
	ds_read_b128 v[212:215], v188 offset:54272
	ds_read_b128 v[224:227], v188 offset:55296
	ds_read_b128 v[228:231], v188 offset:56320
	global_load_lds_dwordx4 v162, s[76:77]
	s_add_i32 m0, s17, 0x2000
	s_add_i32 s17, s67, s29
	global_load_lds_dwordx4 v166, s[76:77]
	s_add_u32 s76, s76, 0x20000
	s_addc_u32 s77, s77, 0
	s_mov_b32 m0, s17
	s_nop 0
	global_load_lds_dwordx4 v162, s[76:77]
	s_add_i32 m0, s17, 0x2000
	s_and_b64 s[36:37], s[36:37], exec
	s_cselect_b32 s36, s22, s34
	s_cselect_b32 s17, s23, s35
	s_add_u32 s36, s36, s74
	s_addc_u32 s37, s17, s75
	global_load_lds_dwordx4 v166, s[76:77]
	s_mov_b32 m0, s56
	s_nop 0
	global_load_lds_dwordx4 v160, s[36:37]
	s_mov_b32 m0, s57
	s_nop 0
	global_load_lds_dwordx4 v164, s[36:37]
	s_waitcnt vmcnt(8)
	s_waitcnt lgkmcnt(0)
	s_barrier
	s_setprio 1
	s_waitcnt lgkmcnt(0)
	v_mfma_f32_16x16x128_f8f6f4 v[92:95], v[24:31], v[192:199], v[92:95]
	v_mfma_f32_16x16x128_f8f6f4 v[84:87], v[16:23], v[192:199], v[84:87]
	v_mfma_f32_16x16x128_f8f6f4 v[76:79], v[24:31], v[200:207], v[76:79]
	v_mfma_f32_16x16x128_f8f6f4 v[64:67], v[16:23], v[200:207], v[64:67]
	v_mfma_f32_16x16x128_f8f6f4 v[52:55], v[24:31], v[208:215], v[52:55]
	v_mfma_f32_16x16x128_f8f6f4 v[44:47], v[16:23], v[208:215], v[44:47]
	v_mfma_f32_16x16x128_f8f6f4 v[36:39], v[24:31], v[224:231], v[36:39]
	v_mfma_f32_16x16x128_f8f6f4 v[32:35], v[16:23], v[224:231], v[32:35]
	s_setprio 0
	s_setprio 1
	v_mfma_f32_16x16x128_f8f6f4 v[88:91], v[8:15], v[192:199], v[88:91]
	v_mfma_f32_16x16x128_f8f6f4 v[80:83], v[0:7], v[192:199], v[80:83]
	v_mfma_f32_16x16x128_f8f6f4 v[68:71], v[8:15], v[200:207], v[68:71]
	v_mfma_f32_16x16x128_f8f6f4 v[56:59], v[0:7], v[200:207], v[56:59]
	v_mfma_f32_16x16x128_f8f6f4 v[72:75], v[8:15], v[208:215], v[72:75]
	v_mfma_f32_16x16x128_f8f6f4 v[60:63], v[0:7], v[208:215], v[60:63]
	v_mfma_f32_16x16x128_f8f6f4 v[48:51], v[8:15], v[224:231], v[48:51]
	v_mfma_f32_16x16x128_f8f6f4 v[40:43], v[0:7], v[224:231], v[40:43]
	s_setprio 0
	s_barrier
	v_lshl_add_u64 v[178:179], v[178:179], 0, s[6:7]
	v_lshl_add_u64 v[180:181], v[180:181], 0, s[6:7]
	s_add_i32 s15, s15, 2
	s_and_b64 vcc, exec, s[40:41]
	s_cbranch_vccnz .LBB0_594
	s_andn2_b64 vcc, exec, s[12:13]
	s_cbranch_vccnz .LBB0_597
	s_barrier
